# v81 + grid barrier leader path: dropped the two vmcnt(0) waits that only served the hoisted invalidate (before and after the leader's local release add)
# speedup vs baseline: 1.0167x; 1.0090x over previous
; __device__ __forceinline__ unsigned xb_ld(unsigned* p)              { return __hip_atomic_load(p, __ATOMIC_RELAXED, __HIP_MEMORY_SCOPE_AGENT); }
; __device__ __forceinline__ unsigned xb_add(unsigned* p, unsigned v) { return __hip_atomic_fetch_add(p, v, __ATOMIC_RELAXED, __HIP_MEMORY_SCOPE_AGENT); }
; #define XB_SPIN(cond, bar) do { unsigned _sp = 0; while (cond) { __builtin_amdgcn_s_sleep(1); \
;     if ((++_sp & 255u) == 0u) { if (xb_ld(&(bar)[XB_TMO])) break; if (_sp > XB_SPIN_CAP) { atomicAdd(&(bar)[XB_TMO], 1u); break; } } } } while (0)
; __device__ __forceinline__ void xcd_barrier(const XcdBarrier& b) {
;     ...
;             __builtin_amdgcn_fence(__ATOMIC_ACQUIRE, "agent");
;             xb_add(&bar[XB_XGEN(b.x)], 1u);
;             asm volatile("s_waitcnt vmcnt(0)" ::: "memory");
;         } else {
;             XB_SPIN(xb_ld(&bar[XB_XGEN(b.x)]) == gen, bar);
;             __builtin_amdgcn_fence(__ATOMIC_ACQUIRE, "agent");
;             asm volatile("s_waitcnt vmcnt(0)" ::: "memory");
;         }
;     }
;     __syncthreads();
.LBB0_239:
	s_or_b64 exec, exec, s[10:11]
	s_mov_b64 s[10:11], exec
	v_mbcnt_lo_u32_b32 v1, s10, 0
	v_mbcnt_hi_u32_b32 v1, s11, v1
	v_cmp_eq_u32_e32 vcc, 0, v1
	s_and_saveexec_b64 s[12:13], vcc
	s_cbranch_execz .LBB0_241
	s_bcnt1_i32_b64 s2, s[10:11]
	v_mov_b32_e32 v1, 0x2000
	v_mov_b32_e32 v2, s2
	global_atomic_add v1, v2, s[6:7] offset:1024
.LBB0_241:
	s_or_b64 exec, exec, s[12:13]
.LBB0_242:
	s_or_b64 exec, exec, s[4:5]
	s_waitcnt lgkmcnt(0)
	s_barrier

; __device__ __forceinline__ unsigned xb_ld(unsigned* p)              { return __hip_atomic_load(p, __ATOMIC_RELAXED, __HIP_MEMORY_SCOPE_AGENT); }
; __device__ __forceinline__ unsigned xb_add(unsigned* p, unsigned v) { return __hip_atomic_fetch_add(p, v, __ATOMIC_RELAXED, __HIP_MEMORY_SCOPE_AGENT); }
; #define XB_SPIN(cond, bar) do { unsigned _sp = 0; while (cond) { __builtin_amdgcn_s_sleep(1); \
;     if ((++_sp & 255u) == 0u) { if (xb_ld(&(bar)[XB_TMO])) break; if (_sp > XB_SPIN_CAP) { atomicAdd(&(bar)[XB_TMO], 1u); break; } } } } while (0)
; __device__ __forceinline__ void xcd_barrier(const XcdBarrier& b) {
;     ...
;             __builtin_amdgcn_fence(__ATOMIC_ACQUIRE, "agent");
;             xb_add(&bar[XB_XGEN(b.x)], 1u);
;             asm volatile("s_waitcnt vmcnt(0)" ::: "memory");
;         } else {
;             XB_SPIN(xb_ld(&bar[XB_XGEN(b.x)]) == gen, bar);
;             __builtin_amdgcn_fence(__ATOMIC_ACQUIRE, "agent");
;             asm volatile("s_waitcnt vmcnt(0)" ::: "memory");
;         }
;     }
;     __syncthreads();
.LBB0_384:
	s_or_b64 exec, exec, s[8:9]
	s_mov_b64 s[8:9], exec
	v_mbcnt_lo_u32_b32 v1, s8, 0
	v_mbcnt_hi_u32_b32 v1, s9, v1
	v_cmp_eq_u32_e32 vcc, 0, v1
	s_and_saveexec_b64 s[10:11], vcc
	s_cbranch_execz .LBB0_386
	s_bcnt1_i32_b64 s2, s[8:9]
	v_mov_b32_e32 v1, 0x2000
	v_mov_b32_e32 v2, s2
	global_atomic_add v1, v2, s[6:7] offset:1024
.LBB0_386:
	s_or_b64 exec, exec, s[10:11]
.LBB0_387:
	s_or_b64 exec, exec, s[0:1]
	s_waitcnt lgkmcnt(0)
	s_barrier

; __device__ __forceinline__ unsigned xb_ld(unsigned* p)              { return __hip_atomic_load(p, __ATOMIC_RELAXED, __HIP_MEMORY_SCOPE_AGENT); }
; __device__ __forceinline__ unsigned xb_add(unsigned* p, unsigned v) { return __hip_atomic_fetch_add(p, v, __ATOMIC_RELAXED, __HIP_MEMORY_SCOPE_AGENT); }
; #define XB_SPIN(cond, bar) do { unsigned _sp = 0; while (cond) { __builtin_amdgcn_s_sleep(1); \
;     if ((++_sp & 255u) == 0u) { if (xb_ld(&(bar)[XB_TMO])) break; if (_sp > XB_SPIN_CAP) { atomicAdd(&(bar)[XB_TMO], 1u); break; } } } } while (0)
; __device__ __forceinline__ void xcd_barrier(const XcdBarrier& b) {
;     ...
;             __builtin_amdgcn_fence(__ATOMIC_ACQUIRE, "agent");
;             xb_add(&bar[XB_XGEN(b.x)], 1u);
;             asm volatile("s_waitcnt vmcnt(0)" ::: "memory");
;         } else {
;             XB_SPIN(xb_ld(&bar[XB_XGEN(b.x)]) == gen, bar);
;             __builtin_amdgcn_fence(__ATOMIC_ACQUIRE, "agent");
;             asm volatile("s_waitcnt vmcnt(0)" ::: "memory");
;         }
;     }
;     __syncthreads();
.LBB0_542:
	s_or_b64 exec, exec, s[6:7]
	s_mov_b64 s[6:7], exec
	v_mbcnt_lo_u32_b32 v1, s6, 0
	v_mbcnt_hi_u32_b32 v1, s7, v1
	v_cmp_eq_u32_e32 vcc, 0, v1
	s_and_saveexec_b64 s[8:9], vcc
	s_cbranch_execz .LBB0_544
	s_bcnt1_i32_b64 s2, s[6:7]
	v_mov_b32_e32 v1, 0x2000
	v_mov_b32_e32 v2, s2
	global_atomic_add v1, v2, s[4:5] offset:1024
.LBB0_544:
	s_or_b64 exec, exec, s[8:9]
.LBB0_545:
	s_or_b64 exec, exec, s[0:1]
	s_waitcnt lgkmcnt(0)
	s_barrier

; __device__ __forceinline__ unsigned xb_ld(unsigned* p)              { return __hip_atomic_load(p, __ATOMIC_RELAXED, __HIP_MEMORY_SCOPE_AGENT); }
; __device__ __forceinline__ unsigned xb_add(unsigned* p, unsigned v) { return __hip_atomic_fetch_add(p, v, __ATOMIC_RELAXED, __HIP_MEMORY_SCOPE_AGENT); }
; #define XB_SPIN(cond, bar) do { unsigned _sp = 0; while (cond) { __builtin_amdgcn_s_sleep(1); \
;     if ((++_sp & 255u) == 0u) { if (xb_ld(&(bar)[XB_TMO])) break; if (_sp > XB_SPIN_CAP) { atomicAdd(&(bar)[XB_TMO], 1u); break; } } } } while (0)
; __device__ __forceinline__ void xcd_barrier(const XcdBarrier& b) {
;     ...
;             xb_add(&bar[XB_XGEN(b.x)], 1u);
;             asm volatile("s_waitcnt vmcnt(0)" ::: "memory");
;         } else {
;             XB_SPIN(xb_ld(&bar[XB_XGEN(b.x)]) == gen, bar);
;             __builtin_amdgcn_fence(__ATOMIC_ACQUIRE, "agent");
;             asm volatile("s_waitcnt vmcnt(0)" ::: "memory");
;         }
;     }
;     __syncthreads();
.LBB0_612:
	s_or_b64 exec, exec, s[10:11]
.LBB0_613:
	s_or_b64 exec, exec, s[0:1]
	s_waitcnt lgkmcnt(0)
	s_barrier

; __device__ __forceinline__ unsigned xb_ld(unsigned* p)              { return __hip_atomic_load(p, __ATOMIC_RELAXED, __HIP_MEMORY_SCOPE_AGENT); }
; __device__ __forceinline__ unsigned xb_add(unsigned* p, unsigned v) { return __hip_atomic_fetch_add(p, v, __ATOMIC_RELAXED, __HIP_MEMORY_SCOPE_AGENT); }
; #define XB_SPIN(cond, bar) do { unsigned _sp = 0; while (cond) { __builtin_amdgcn_s_sleep(1); \
;     if ((++_sp & 255u) == 0u) { if (xb_ld(&(bar)[XB_TMO])) break; if (_sp > XB_SPIN_CAP) { atomicAdd(&(bar)[XB_TMO], 1u); break; } } } } while (0)
; __device__ __forceinline__ void xcd_barrier(const XcdBarrier& b) {
;     ...
;             xb_add(&bar[XB_XGEN(b.x)], 1u);
;             asm volatile("s_waitcnt vmcnt(0)" ::: "memory");
;         } else {
;             XB_SPIN(xb_ld(&bar[XB_XGEN(b.x)]) == gen, bar);
;             __builtin_amdgcn_fence(__ATOMIC_ACQUIRE, "agent");
;             asm volatile("s_waitcnt vmcnt(0)" ::: "memory");
;         }
;     }
;     __syncthreads();
.LBB0_709:
	s_or_b64 exec, exec, s[10:11]
.LBB0_710:
	s_or_b64 exec, exec, s[0:1]
	s_waitcnt lgkmcnt(0)
	s_barrier

; __device__ __forceinline__ unsigned xb_ld(unsigned* p)              { return __hip_atomic_load(p, __ATOMIC_RELAXED, __HIP_MEMORY_SCOPE_AGENT); }
; __device__ __forceinline__ unsigned xb_add(unsigned* p, unsigned v) { return __hip_atomic_fetch_add(p, v, __ATOMIC_RELAXED, __HIP_MEMORY_SCOPE_AGENT); }
; #define XB_SPIN(cond, bar) do { unsigned _sp = 0; while (cond) { __builtin_amdgcn_s_sleep(1); \
;     if ((++_sp & 255u) == 0u) { if (xb_ld(&(bar)[XB_TMO])) break; if (_sp > XB_SPIN_CAP) { atomicAdd(&(bar)[XB_TMO], 1u); break; } } } } while (0)
; __device__ __forceinline__ void xcd_barrier(const XcdBarrier& b) {
;     ...
;             xb_add(&bar[XB_XGEN(b.x)], 1u);
;             asm volatile("s_waitcnt vmcnt(0)" ::: "memory");
;         } else {
;             XB_SPIN(xb_ld(&bar[XB_XGEN(b.x)]) == gen, bar);
;             __builtin_amdgcn_fence(__ATOMIC_ACQUIRE, "agent");
;             asm volatile("s_waitcnt vmcnt(0)" ::: "memory");
;         }
;     }
;     __syncthreads();
.LBB0_831:
	s_or_b64 exec, exec, s[10:11]
.LBB0_832:
	s_or_b64 exec, exec, s[0:1]
	s_waitcnt lgkmcnt(0)
	s_barrier

; __device__ __forceinline__ unsigned xb_ld(unsigned* p)              { return __hip_atomic_load(p, __ATOMIC_RELAXED, __HIP_MEMORY_SCOPE_AGENT); }
; __device__ __forceinline__ unsigned xb_add(unsigned* p, unsigned v) { return __hip_atomic_fetch_add(p, v, __ATOMIC_RELAXED, __HIP_MEMORY_SCOPE_AGENT); }
; #define XB_SPIN(cond, bar) do { unsigned _sp = 0; while (cond) { __builtin_amdgcn_s_sleep(1); \
;     if ((++_sp & 255u) == 0u) { if (xb_ld(&(bar)[XB_TMO])) break; if (_sp > XB_SPIN_CAP) { atomicAdd(&(bar)[XB_TMO], 1u); break; } } } } while (0)
; __device__ __forceinline__ void xcd_barrier(const XcdBarrier& b) {
;     ...
;             xb_add(&bar[XB_XGEN(b.x)], 1u);
;             asm volatile("s_waitcnt vmcnt(0)" ::: "memory");
;         } else {
;             XB_SPIN(xb_ld(&bar[XB_XGEN(b.x)]) == gen, bar);
;             __builtin_amdgcn_fence(__ATOMIC_ACQUIRE, "agent");
;             asm volatile("s_waitcnt vmcnt(0)" ::: "memory");
;         }
;     }
;     __syncthreads();
.LBB0_932:
	s_or_b64 exec, exec, s[8:9]
.LBB0_933:
	s_or_b64 exec, exec, s[0:1]
	s_waitcnt lgkmcnt(0)
	s_barrier

; __device__ __forceinline__ unsigned xb_ld(unsigned* p)              { return __hip_atomic_load(p, __ATOMIC_RELAXED, __HIP_MEMORY_SCOPE_AGENT); }
; __device__ __forceinline__ unsigned xb_add(unsigned* p, unsigned v) { return __hip_atomic_fetch_add(p, v, __ATOMIC_RELAXED, __HIP_MEMORY_SCOPE_AGENT); }
; #define XB_SPIN(cond, bar) do { unsigned _sp = 0; while (cond) { __builtin_amdgcn_s_sleep(1); \
;     if ((++_sp & 255u) == 0u) { if (xb_ld(&(bar)[XB_TMO])) break; if (_sp > XB_SPIN_CAP) { atomicAdd(&(bar)[XB_TMO], 1u); break; } } } } while (0)
; __device__ __forceinline__ void xcd_barrier(const XcdBarrier& b) {
;     ...
;             xb_add(&bar[XB_XGEN(b.x)], 1u);
;             asm volatile("s_waitcnt vmcnt(0)" ::: "memory");
;         } else {
;             XB_SPIN(xb_ld(&bar[XB_XGEN(b.x)]) == gen, bar);
;             __builtin_amdgcn_fence(__ATOMIC_ACQUIRE, "agent");
;             asm volatile("s_waitcnt vmcnt(0)" ::: "memory");
;         }
;     }
;     __syncthreads();
.LBB0_1077:
	s_or_b64 exec, exec, s[10:11]
.LBB0_1078:
	s_or_b64 exec, exec, s[0:1]
	s_waitcnt lgkmcnt(0)
	s_barrier

; __device__ __forceinline__ unsigned xb_ld(unsigned* p)              { return __hip_atomic_load(p, __ATOMIC_RELAXED, __HIP_MEMORY_SCOPE_AGENT); }
; __device__ __forceinline__ unsigned xb_add(unsigned* p, unsigned v) { return __hip_atomic_fetch_add(p, v, __ATOMIC_RELAXED, __HIP_MEMORY_SCOPE_AGENT); }
; #define XB_SPIN(cond, bar) do { unsigned _sp = 0; while (cond) { __builtin_amdgcn_s_sleep(1); \
;     if ((++_sp & 255u) == 0u) { if (xb_ld(&(bar)[XB_TMO])) break; if (_sp > XB_SPIN_CAP) { atomicAdd(&(bar)[XB_TMO], 1u); break; } } } } while (0)
; __device__ __forceinline__ void xcd_barrier(const XcdBarrier& b) {
;     ...
;             xb_add(&bar[XB_XGEN(b.x)], 1u);
;             asm volatile("s_waitcnt vmcnt(0)" ::: "memory");
;         } else {
;             XB_SPIN(xb_ld(&bar[XB_XGEN(b.x)]) == gen, bar);
;             __builtin_amdgcn_fence(__ATOMIC_ACQUIRE, "agent");
;             asm volatile("s_waitcnt vmcnt(0)" ::: "memory");
;         }
;     }
;     __syncthreads();
.LBB0_1235:
	s_or_b64 exec, exec, s[8:9]
.LBB0_1236:
	s_or_b64 exec, exec, s[0:1]
	s_waitcnt lgkmcnt(0)
	s_barrier

; __device__ __forceinline__ unsigned xb_ld(unsigned* p)              { return __hip_atomic_load(p, __ATOMIC_RELAXED, __HIP_MEMORY_SCOPE_AGENT); }
; __device__ __forceinline__ unsigned xb_add(unsigned* p, unsigned v) { return __hip_atomic_fetch_add(p, v, __ATOMIC_RELAXED, __HIP_MEMORY_SCOPE_AGENT); }
; #define XB_SPIN(cond, bar) do { unsigned _sp = 0; while (cond) { __builtin_amdgcn_s_sleep(1); \
;     if ((++_sp & 255u) == 0u) { if (xb_ld(&(bar)[XB_TMO])) break; if (_sp > XB_SPIN_CAP) { atomicAdd(&(bar)[XB_TMO], 1u); break; } } } } while (0)
; __device__ __forceinline__ void xcd_barrier(const XcdBarrier& b) {
;     ...
;             xb_add(&bar[XB_XGEN(b.x)], 1u);
;             asm volatile("s_waitcnt vmcnt(0)" ::: "memory");
;         } else {
;             XB_SPIN(xb_ld(&bar[XB_XGEN(b.x)]) == gen, bar);
;             __builtin_amdgcn_fence(__ATOMIC_ACQUIRE, "agent");
;             asm volatile("s_waitcnt vmcnt(0)" ::: "memory");
;         }
;     }
;     __syncthreads();
.LBB0_1302:
	s_or_b64 exec, exec, s[10:11]
.LBB0_1303:
	s_or_b64 exec, exec, s[0:1]
	s_waitcnt lgkmcnt(0)
	s_barrier

; __device__ __forceinline__ unsigned xb_ld(unsigned* p)              { return __hip_atomic_load(p, __ATOMIC_RELAXED, __HIP_MEMORY_SCOPE_AGENT); }
; __device__ __forceinline__ unsigned xb_add(unsigned* p, unsigned v) { return __hip_atomic_fetch_add(p, v, __ATOMIC_RELAXED, __HIP_MEMORY_SCOPE_AGENT); }
; #define XB_SPIN(cond, bar) do { unsigned _sp = 0; while (cond) { __builtin_amdgcn_s_sleep(1); \
;     if ((++_sp & 255u) == 0u) { if (xb_ld(&(bar)[XB_TMO])) break; if (_sp > XB_SPIN_CAP) { atomicAdd(&(bar)[XB_TMO], 1u); break; } } } } while (0)
; __device__ __forceinline__ void xcd_barrier(const XcdBarrier& b) {
;     ...
;             xb_add(&bar[XB_XGEN(b.x)], 1u);
;             asm volatile("s_waitcnt vmcnt(0)" ::: "memory");
;         } else {
;             XB_SPIN(xb_ld(&bar[XB_XGEN(b.x)]) == gen, bar);
;             __builtin_amdgcn_fence(__ATOMIC_ACQUIRE, "agent");
;             asm volatile("s_waitcnt vmcnt(0)" ::: "memory");
;         }
;     }
;     __syncthreads();
.LBB0_1399:
	s_or_b64 exec, exec, s[10:11]
.LBB0_1400:
	s_or_b64 exec, exec, s[0:1]
	s_waitcnt lgkmcnt(0)
	s_barrier

; __device__ __forceinline__ unsigned xb_ld(unsigned* p)              { return __hip_atomic_load(p, __ATOMIC_RELAXED, __HIP_MEMORY_SCOPE_AGENT); }
; __device__ __forceinline__ unsigned xb_add(unsigned* p, unsigned v) { return __hip_atomic_fetch_add(p, v, __ATOMIC_RELAXED, __HIP_MEMORY_SCOPE_AGENT); }
; #define XB_SPIN(cond, bar) do { unsigned _sp = 0; while (cond) { __builtin_amdgcn_s_sleep(1); \
;     if ((++_sp & 255u) == 0u) { if (xb_ld(&(bar)[XB_TMO])) break; if (_sp > XB_SPIN_CAP) { atomicAdd(&(bar)[XB_TMO], 1u); break; } } } } while (0)
; __device__ __forceinline__ void xcd_barrier(const XcdBarrier& b) {
;     ...
;             xb_add(&bar[XB_XGEN(b.x)], 1u);
;             asm volatile("s_waitcnt vmcnt(0)" ::: "memory");
;         } else {
;             XB_SPIN(xb_ld(&bar[XB_XGEN(b.x)]) == gen, bar);
;             __builtin_amdgcn_fence(__ATOMIC_ACQUIRE, "agent");
;             asm volatile("s_waitcnt vmcnt(0)" ::: "memory");
;         }
;     }
;     __syncthreads();
.LBB0_1491:
	s_or_b64 exec, exec, s[10:11]
.LBB0_1492:
	s_or_b64 exec, exec, s[0:1]
	s_waitcnt lgkmcnt(0)
	s_barrier

; __device__ __forceinline__ unsigned xb_ld(unsigned* p)              { return __hip_atomic_load(p, __ATOMIC_RELAXED, __HIP_MEMORY_SCOPE_AGENT); }
; __device__ __forceinline__ unsigned xb_add(unsigned* p, unsigned v) { return __hip_atomic_fetch_add(p, v, __ATOMIC_RELAXED, __HIP_MEMORY_SCOPE_AGENT); }
; #define XB_SPIN(cond, bar) do { unsigned _sp = 0; while (cond) { __builtin_amdgcn_s_sleep(1); \
;     if ((++_sp & 255u) == 0u) { if (xb_ld(&(bar)[XB_TMO])) break; if (_sp > XB_SPIN_CAP) { atomicAdd(&(bar)[XB_TMO], 1u); break; } } } } while (0)
; __device__ __forceinline__ void xcd_barrier(const XcdBarrier& b) {
;     ...
;             __builtin_amdgcn_fence(__ATOMIC_ACQUIRE, "agent");
;             xb_add(&bar[XB_XGEN(b.x)], 1u);
;             asm volatile("s_waitcnt vmcnt(0)" ::: "memory");
;         } else {
;             XB_SPIN(xb_ld(&bar[XB_XGEN(b.x)]) == gen, bar);
;             __builtin_amdgcn_fence(__ATOMIC_ACQUIRE, "agent");
;             asm volatile("s_waitcnt vmcnt(0)" ::: "memory");
;         }
;     }
;     __syncthreads();
.LBB0_1704:
	s_or_b64 exec, exec, s[10:11]
	s_mov_b64 s[10:11], exec
	v_mbcnt_lo_u32_b32 v1, s10, 0
	v_mbcnt_hi_u32_b32 v1, s11, v1
	v_cmp_eq_u32_e32 vcc, 0, v1
	s_and_saveexec_b64 s[22:23], vcc
	s_cbranch_execz .LBB0_1706
	s_bcnt1_i32_b64 s2, s[10:11]
	v_mov_b32_e32 v1, 0x2000
	v_mov_b32_e32 v2, s2
	global_atomic_add v1, v2, s[8:9] offset:1024
.LBB0_1706:
	s_or_b64 exec, exec, s[22:23]
.LBB0_1707:
	s_or_b64 exec, exec, s[6:7]
	s_waitcnt lgkmcnt(0)
	s_barrier

; __device__ __forceinline__ unsigned xb_ld(unsigned* p)              { return __hip_atomic_load(p, __ATOMIC_RELAXED, __HIP_MEMORY_SCOPE_AGENT); }
; __device__ __forceinline__ unsigned xb_add(unsigned* p, unsigned v) { return __hip_atomic_fetch_add(p, v, __ATOMIC_RELAXED, __HIP_MEMORY_SCOPE_AGENT); }
; #define XB_SPIN(cond, bar) do { unsigned _sp = 0; while (cond) { __builtin_amdgcn_s_sleep(1); \
;     if ((++_sp & 255u) == 0u) { if (xb_ld(&(bar)[XB_TMO])) break; if (_sp > XB_SPIN_CAP) { atomicAdd(&(bar)[XB_TMO], 1u); break; } } } } while (0)
; __device__ __forceinline__ void xcd_barrier(const XcdBarrier& b) {
;     ...
;             xb_add(&bar[XB_XGEN(b.x)], 1u);
;             asm volatile("s_waitcnt vmcnt(0)" ::: "memory");
;         } else {
;             XB_SPIN(xb_ld(&bar[XB_XGEN(b.x)]) == gen, bar);
;             __builtin_amdgcn_fence(__ATOMIC_ACQUIRE, "agent");
;             asm volatile("s_waitcnt vmcnt(0)" ::: "memory");
;         }
;     }
;     __syncthreads();
.LBB0_1799:
	s_or_b64 exec, exec, s[10:11]
.LBB0_1800:
	s_or_b64 exec, exec, s[4:5]
	s_waitcnt lgkmcnt(0)
	s_barrier

; __device__ __forceinline__ unsigned xb_ld(unsigned* p)              { return __hip_atomic_load(p, __ATOMIC_RELAXED, __HIP_MEMORY_SCOPE_AGENT); }
; __device__ __forceinline__ unsigned xb_add(unsigned* p, unsigned v) { return __hip_atomic_fetch_add(p, v, __ATOMIC_RELAXED, __HIP_MEMORY_SCOPE_AGENT); }
; #define XB_SPIN(cond, bar) do { unsigned _sp = 0; while (cond) { __builtin_amdgcn_s_sleep(1); \
;     if ((++_sp & 255u) == 0u) { if (xb_ld(&(bar)[XB_TMO])) break; if (_sp > XB_SPIN_CAP) { atomicAdd(&(bar)[XB_TMO], 1u); break; } } } } while (0)
; __device__ __forceinline__ void xcd_barrier(const XcdBarrier& b) {
;     ...
;             __builtin_amdgcn_fence(__ATOMIC_ACQUIRE, "agent");
;             xb_add(&bar[XB_XGEN(b.x)], 1u);
;             asm volatile("s_waitcnt vmcnt(0)" ::: "memory");
;         } else {
;             XB_SPIN(xb_ld(&bar[XB_XGEN(b.x)]) == gen, bar);
;             __builtin_amdgcn_fence(__ATOMIC_ACQUIRE, "agent");
;             asm volatile("s_waitcnt vmcnt(0)" ::: "memory");
;         }
;     }
;     __syncthreads();
.LBB0_1901:
	s_or_b64 exec, exec, s[10:11]
	s_mov_b64 s[10:11], exec
	v_mbcnt_lo_u32_b32 v1, s10, 0
	v_mbcnt_hi_u32_b32 v1, s11, v1
	v_cmp_eq_u32_e32 vcc, 0, v1
	s_and_saveexec_b64 s[14:15], vcc
	s_cbranch_execz .LBB0_1903
	s_bcnt1_i32_b64 s2, s[10:11]
	v_mov_b32_e32 v1, 0x2000
	v_mov_b32_e32 v2, s2
	global_atomic_add v1, v2, s[8:9] offset:1024
.LBB0_1903:
	s_or_b64 exec, exec, s[14:15]
.LBB0_1904:
	s_or_b64 exec, exec, s[6:7]
	s_waitcnt lgkmcnt(0)
	s_barrier
